# gemm: static bias rows for GEMM2 are read from LDS before the wait+barrier so their latency hides behind the barrier
# speedup vs baseline: 1.0006x; 1.0006x over previous
.LBB2_7:
	ds_read_b128 v[2:5], v101 offset:1024
	ds_read_b128 v[6:9], v101 offset:1040
	ds_read_b128 v[10:13], v101 offset:1056
	ds_read_b128 v[14:17], v101 offset:1072
	s_waitcnt lgkmcnt(0)
	s_barrier
	ds_read_b128 v[18:21], v99 offset:32768
	ds_read_b128 v[22:25], v99 offset:33792
	v_lshlrev_b32_e32 v97, 5, v94
	v_lshlrev_b32_e32 v95, 2, v95
	s_waitcnt lgkmcnt(0)
	v_mfma_scale_f32_32x32x64_f8f6f4 v[18:33], v[42:49], v[18:25], v[2:17], v96, v96 op_sel_hi:[0,0,0]
	ds_read_b128 v[102:105], v99 offset:34816
	ds_read_b128 v[106:109], v99 offset:35840
	v_lshlrev_b32_e32 v94, 1, v94
	s_mov_b32 s12, 0x10200
	v_and_b32_e32 v94, 4, v94
	s_waitcnt lgkmcnt(0)
	v_mfma_scale_f32_32x32x64_f8f6f4 v[18:33], v[58:65], v[102:109], v[18:33], v96, v96 op_sel_hi:[0,0,0]
	v_add_u32_e32 v102, 0xffffff80, v97
	v_or_b32_e32 v103, v102, v95
	v_mul_u32_u24_e32 v104, 0x108, v1
	v_lshlrev_b32_e32 v103, 1, v103
	v_or_b32_e32 v114, 0xc000, v104
	v_and_b32_e32 v110, 0x48, v103
	v_ashrrev_i32_e32 v111, 4, v102
	ds_read_b128 v[102:105], v99 offset:36864
	ds_read_b128 v[106:109], v99 offset:37888
	v_and_b32_e32 v111, 0x7ffffffc, v111
	v_add_lshl_u32 v115, v110, v111, 1
	v_or_b32_e32 v95, v95, v97
	v_lshlrev_b32_e32 v95, 1, v95
	v_add_u32_e32 v116, 32, v115
	v_add_u32_e32 v117, 64, v115
	v_and_b32_e32 v95, 0x48, v95
	s_waitcnt lgkmcnt(0)
	v_mfma_scale_f32_32x32x64_f8f6f4 v[18:33], v[74:81], v[102:109], v[18:33], v96, v96 op_sel_hi:[0,0,0]
	ds_read_b128 v[106:109], v99 offset:38912
	ds_read_b128 v[110:113], v99 offset:39936
	v_add_u32_e32 v105, 0x60, v115
	v_mul_u32_u24_e32 v102, 0x84, v1
	v_add3_u32 v95, v102, v95, s12
	v_add_u32_e32 v102, v114, v115
	v_add_u32_e32 v103, v114, v116
	v_add_u32_e32 v104, v114, v117
	v_add_u32_e32 v105, v114, v105
	s_waitcnt lgkmcnt(0)
	v_mfma_scale_f32_32x32x64_f8f6f4 v[18:33], v[82:89], v[106:113], v[18:33], v96, v96 op_sel_hi:[0,0,0]
	s_and_saveexec_b64 s[12:13], s[6:7]
	s_xor_b64 s[12:13], exec, s[12:13]
	s_cbranch_execnz .LBB2_10
	s_or_saveexec_b64 s[12:13], s[12:13]
	v_add_u32_e32 v106, v95, v94
	s_xor_b64 exec, exec, s[12:13]
	s_cbranch_execnz .LBB2_11

.LBB2_31:
	ds_read_b128 v[2:5], v101 offset:1024
	ds_read_b128 v[6:9], v101 offset:1040
	ds_read_b128 v[10:13], v101 offset:1056
	ds_read_b128 v[14:17], v101 offset:1072
	s_waitcnt lgkmcnt(0)
	s_barrier
	ds_read_b128 v[18:21], v99 offset:32768
	ds_read_b128 v[22:25], v99 offset:33792
	s_waitcnt lgkmcnt(0)
	v_mfma_scale_f32_32x32x64_f8f6f4 v[18:33], v[42:49], v[18:25], v[2:17], v110, v110 op_sel_hi:[0,0,0]
	ds_read_b128 v[116:119], v99 offset:34816
	ds_read_b128 v[120:123], v99 offset:35840
	s_waitcnt lgkmcnt(0)
	v_mfma_scale_f32_32x32x64_f8f6f4 v[18:33], v[58:65], v[116:123], v[18:33], v110, v110 op_sel_hi:[0,0,0]
	ds_read_b128 v[116:119], v99 offset:36864
	ds_read_b128 v[120:123], v99 offset:37888
	s_waitcnt lgkmcnt(0)
	v_mfma_scale_f32_32x32x64_f8f6f4 v[18:33], v[74:81], v[116:123], v[18:33], v110, v110 op_sel_hi:[0,0,0]
	ds_read_b128 v[116:119], v99 offset:38912
	ds_read_b128 v[120:123], v99 offset:39936
	s_waitcnt lgkmcnt(0)
	v_mfma_scale_f32_32x32x64_f8f6f4 v[18:33], v[82:89], v[116:123], v[18:33], v110, v110 op_sel_hi:[0,0,0]
	s_and_saveexec_b64 s[12:13], s[6:7]
	s_xor_b64 s[12:13], exec, s[12:13]
	s_cbranch_execnz .LBB2_34
	s_andn2_saveexec_b64 s[12:13], s[12:13]
	s_cbranch_execnz .LBB2_35
